# baseline (speedup 1.0000x reference)
_Z11prep_kernelPKfS0_S0_S0_PDF16_S1_S0_S1_:
	s_load_dwordx8 s[4:11], s[0:1], 0x0
	s_load_dwordx4 s[12:15], s[0:1], 0x20
	s_mov_b32 s3, 0
	s_lshl_b64 s[2:3], s[2:3], 6
	v_mov_b32_e32 v187, v0
	v_cmp_gt_u32_e32 vcc, 8, v0
	v_lshlrev_b32_e32 v1, 3, v0
	s_and_saveexec_b64 s[16:17], vcc
	s_cbranch_execz .LBB0_2
	s_load_dwordx4 s[20:23], s[0:1], 0x30
	v_or_b32_e32 v10, s2, v1
	v_mov_b32_e32 v11, s3
	s_waitcnt lgkmcnt(0)
	v_lshl_add_u64 v[12:13], v[10:11], 2, s[20:21]
	global_load_dwordx4 v[176:179], v[12:13], off
	global_load_dwordx4 v[180:183], v[12:13], off offset:16
	v_lshl_add_u64 v[184:185], v[10:11], 1, s[22:23]
